# every 1 KB stream piece aligned to a 1 KB boundary (row start aligned down by up to 960 B) instead of 128 B
# baseline (speedup 1.0000x reference)
_Z11attn_kernelPKfS0_PKDv8_DF16_S0_Pfi:
	s_load_dwordx2 s[28:29], s[0:1], 0x0
	v_cmp_gt_u32_e32 vcc, 8, v0
	s_and_saveexec_b64 s[4:5], vcc
	v_lshlrev_b32_e32 v1, 2, v0
	v_mov_b32_e32 v2, 0
	ds_write_b32 v1, v2 offset:36864
	s_or_b64 exec, exec, s[4:5]
	s_load_dword s33, s[0:1], 0x28
	v_bfe_u32 v1, v0, 6, 2
	v_lshl_or_b32 v82, s2, 2, v1
	v_readfirstlane_b32 s34, v0
	s_cmp_gt_u32 s34, 0xff
	s_cbranch_scc1 .Lsc_early_skip
	v_and_b32_e32 v3, 63, v0
	v_lshlrev_b32_e32 v2, 4, v3
	s_lshr_b32 s35, s34, 6
	s_lshl_b32 s37, s2, 2
	s_add_u32 s37, s37, s35
	s_mul_i32 s47, s37, 0x9c4
	s_and_b32 s47, s47, 63
	s_mul_i32 s38, s37, 0x9c40
	s_lshl_b32 s40, s47, 4
	s_sub_u32 s38, s38, s40
	v_max_u32_e32 v12, s47, v3
	v_lshlrev_b32_e32 v12, 4, v12
	s_waitcnt lgkmcnt(0)
	s_and_b32 s29, s29, 0xffff
	s_mov_b32 s30, 0x17d78400
	s_mov_b32 s31, 0x20000
	buffer_load_dwordx4 v[100:103], v12, s[28:31], s38 offen nt
	s_add_u32 s40, s38, 0x400
	buffer_load_dwordx4 v[104:107], v2, s[28:31], s40 offen nt
	s_add_u32 s40, s38, 0x800
	buffer_load_dwordx4 v[108:111], v2, s[28:31], s40 offen nt
	s_add_u32 s40, s38, 0xc00
	buffer_load_dwordx4 v[112:115], v2, s[28:31], s40 offen nt
	s_add_u32 s40, s38, 0x1000
	buffer_load_dwordx4 v[116:119], v2, s[28:31], s40 offen nt
	s_add_u32 s40, s38, 0x1400
	buffer_load_dwordx4 v[120:123], v2, s[28:31], s40 offen nt
	s_add_u32 s40, s38, 0x1800
	buffer_load_dwordx4 v[124:127], v2, s[28:31], s40 offen nt
	s_add_u32 s40, s38, 0x1c00
	buffer_load_dwordx4 v[128:131], v2, s[28:31], s40 offen nt
	s_add_u32 s40, s38, 0x2000
	buffer_load_dwordx4 v[132:135], v2, s[28:31], s40 offen nt
	s_add_u32 s40, s38, 0x2400
	buffer_load_dwordx4 v[136:139], v2, s[28:31], s40 offen nt

.LBB1_217:
	s_andn2_saveexec_b64 s[0:1], s[30:31]
	s_cbranch_execz .LBB1_384
	v_readfirstlane_b32 s34, v1
	v_readfirstlane_b32 s37, v82
	v_readfirstlane_b32 s36, v84
	v_and_b32_e32 v3, 63, v0
	v_lshlrev_b32_e32 v2, 4, v3
	s_cmp_lt_i32 s36, 0
	s_cbranch_scc1 .LBB1_384
	s_waitcnt lgkmcnt(0)
	s_and_b32 s29, s29, 0xffff
	s_mov_b32 s30, 0x17d78400
	s_mov_b32 s31, 0x20000
	s_mov_b32 s35, 0
	s_movk_i32 s7, 0x80
	s_mov_b32 s9, 0x7fffffff
	s_lshl_b32 s44, s34, 12
	s_add_u32 s44, s44, 0x4000
	s_lshl_b32 s45, s34, 10
	s_add_u32 s45, s45, 0x8000
	s_lshl_b32 s46, s34, 3
	s_add_u32 s46, s46, 0x9000
	s_mul_i32 s47, s37, 0x9c4
	s_and_b32 s47, s47, 63
	s_mul_i32 s38, s37, 0x9c40
	s_lshl_b32 s40, s47, 4
	s_sub_u32 s38, s38, s40
	v_max_u32_e32 v12, s47, v3
	v_lshlrev_b32_e32 v12, 4, v12
.Lsc_row:
	v_subrev_u32_e32 v8, s47, v3
	v_lshlrev_b32_e32 v8, 2, v8
	s_add_i32 s41, s47, 3
	v_min_u32_e32 v4, s41, v3
	v_lshlrev_b32_e32 v4, 4, v4
	s_lshl_b64 s[48:49], -1, s47
	s_add_i32 s41, s47, 3
	s_lshl_b64 s[50:51], 2, s41
	s_sub_u32 s50, s50, 1
	s_subb_u32 s51, s51, 0
	s_and_b32 s41, s35, 1
	s_lshl_b32 s40, s41, 11
	s_add_u32 s40, s40, s44
	v_mov_b32_e32 v9, s40
	s_lshl_b32 s40, s41, 9
	s_add_u32 s40, s40, s45
	v_mov_b32_e32 v10, s40
	s_lshl_b32 s40, s41, 2
	s_add_u32 s40, s40, s46
	v_mov_b32_e32 v11, s40
	s_cmp_lt_i32 s35, s36
	s_cbranch_scc0 .Lsc_nonext
	s_add_i32 s52, s37, s33
	s_mul_i32 s53, s52, 0x9c4
	s_and_b32 s53, s53, 63
	s_mul_i32 s39, s52, 0x9c40
	s_lshl_b32 s40, s53, 4
	s_sub_u32 s39, s39, s40
	v_max_u32_e32 v5, s53, v3
	v_lshlrev_b32_e32 v5, 4, v5
	v_mov_b32_e32 v6, v2
	s_add_i32 s40, s53, 3
	v_min_u32_e32 v7, s40, v3
	v_lshlrev_b32_e32 v7, 4, v7
	s_branch .Lsc_gotnext
